# baseline (speedup 1.0000x reference)
.Lno_anc:
	s_or_b64 exec, exec, s[8:9]
	v_mov_b32_e32 v7, 0x80
	s_waitcnt vmcnt(0)
	s_and_saveexec_b64 s[0:1], vcc
	ds_write_b128 v11, v[2:5] offset:32768
	ds_write_b128 v11, v[44:47] offset:40960
	s_or_b64 exec, exec, s[0:1]
	s_sub_u32 s26, 0xff, s2
	s_mul_i32 s26, s26, 0
	s_lshr_b32 s26, s26, 7
	s_min_u32 s26, s26, 64
	s_cmp_eq_u32 s26, 0
	s_cbranch_scc1 .Lhold_done
